# mixer A pass 2: first dil-16 K/V tiles requested before the residue's state loads, first dil-4 tiles requested inside the last dil-16 tile
# speedup vs baseline: 1.0142x; 1.0009x over previous
; #define BA_LOAD(kn, vn, kt_) do { const int kb_ = kb_first + 32 * (kt_); \
;         _Pragma("unroll") for (int ii = 0; ii < 4; ++ii) { const size_t row_ = (size_t)(res + dil * (kb_ + vr + 8 * ii)); \
;             kn[ii] = *(const v4u*)(Kb + row_ * kpitch + 8 * vc); vn[ii] = *(const v4u*)(Vb + row_ * vpitch + 8 * vc); } } while (0)
; #define BA_LOAD(kn, vn, kt_) do { const int kb_ = kb_first + 32 * (kt_); \
;         _Pragma("unroll") for (int ii = 0; ii < 4; ++ii) { const size_t row_ = (size_t)(res + dil * (kb_ + vr + 8 * ii)); \
;             kn[ii] = *(const v4u*)(Kb + row_ * kpitch + 8 * vc); vn[ii] = *(const v4u*)(Vb + row_ * vpitch + 8 * vc); } } while (0)
; __device__ __forceinline__ void band_branch_fast(f32x16& o0, f32x16& o1, f32x4& lsum, unsigned& orw, const bf16x8 (&qf)[4], ...
;     ...
;     if (kt_lo < kt_hi) BA_LOAD(kn, vn, kt_lo);
; __device__ __forceinline__ void mixer_a_phase(const bf16* AQ, const bf16* AK, const bf16* AV  , bf16* O, float* ST, float* ML, const float* rel_bias, LAS unsigned char* lds, int G, int blk, int tid, int lane, int wave) {
;     ...
;             band_state_load(o0, o1, m, l, ST + ((tb0 + tq) * 8 + h) * 64, ML + ((tb0 + tq) * 8 + h) * 2, lane);
;             bool exact = __any(m != M_FAST);
;             if (__builtin_expect(!exact, 1)) {
;                 f32x4 lsum = {0.f, 0.f, 0.f, 0.f}; unsigned orw = 0u;
;                 band_branch_fast(o0, o1, lsum, orw, qf, Kb, 512, Vb, 512, 16, r, 512, 32 * (a - 2), 5, tab + 2 * TA_LEN, -(32 * a + i5) + 64 + TA_OFF + 8 * hh, vst, lane);
.LBB0_387:
	s_and_b64 vcc, exec, s[26:27]
	s_cbranch_vccnz .Lmx_pre4
	v_and_b32_e32 v58, 7, v1
	v_xor_b32_e32 v59, v58, v196
	v_sub_u32_e32 v58, v59, v58
	v_lshlrev_b32_e32 v64, 4, v58
	v_ashrrev_i32_e32 v65, 31, v64
	v_lshl_add_u64 v[66:67], v[152:153], 0, v[64:65]
	v_readlane_b32 s98, v254, 59
	s_mov_b64 s[100:101], 0x80000
	v_add_u32_e32 v58, s25, v219
	v_ashrrev_i32_e32 v59, 31, v58
	v_lshlrev_b64 v[58:59], 10, v[58:59]
	v_lshl_add_u64 v[106:107], v[66:67], 0, v[58:59]
	v_lshl_add_u64 v[108:109], v[154:155], 0, v[58:59]
	v_add_u32_e32 v58, s25, v220
	v_ashrrev_i32_e32 v59, 31, v58
	v_lshlrev_b64 v[58:59], 10, v[58:59]
	v_lshl_add_u64 v[110:111], v[66:67], 0, v[58:59]
	v_lshl_add_u64 v[112:113], v[154:155], 0, v[58:59]
	v_add_u32_e32 v58, s25, v221
	v_ashrrev_i32_e32 v59, 31, v58
	v_lshlrev_b64 v[58:59], 10, v[58:59]
	v_lshl_add_u64 v[114:115], v[66:67], 0, v[58:59]
	v_lshl_add_u64 v[116:117], v[154:155], 0, v[58:59]
	v_add_u32_e32 v58, s25, v222
	v_ashrrev_i32_e32 v59, 31, v58
	v_lshlrev_b64 v[58:59], 10, v[58:59]
	v_lshl_add_u64 v[118:119], v[66:67], 0, v[58:59]
	v_lshl_add_u64 v[120:121], v[154:155], 0, v[58:59]
	s_lshl_b32 s98, s98, 14
	s_add_i32 s98, s98, 0x4000
	s_mov_b32 s99, 0
	s_add_i32 m0, s98, 0x1000
	s_nop 0
	global_load_lds_dwordx4 v[106:107], off
	s_add_i32 m0, s98, 0x0
	v_lshl_add_u64 v[106:107], v[106:107], 0, s[100:101]
	global_load_lds_dwordx4 v[108:109], off
	s_add_i32 m0, s98, 0x1400
	v_lshl_add_u64 v[108:109], v[108:109], 0, s[100:101]
	global_load_lds_dwordx4 v[110:111], off
	s_add_i32 m0, s98, 0x400
	v_lshl_add_u64 v[110:111], v[110:111], 0, s[100:101]
	global_load_lds_dwordx4 v[112:113], off
	s_add_i32 m0, s98, 0x1800
	v_lshl_add_u64 v[112:113], v[112:113], 0, s[100:101]
	global_load_lds_dwordx4 v[114:115], off
	s_add_i32 m0, s98, 0x800
	v_lshl_add_u64 v[114:115], v[114:115], 0, s[100:101]
	global_load_lds_dwordx4 v[116:117], off
	s_add_i32 m0, s98, 0x1c00
	v_lshl_add_u64 v[116:117], v[116:117], 0, s[100:101]
	global_load_lds_dwordx4 v[118:119], off
	s_add_i32 m0, s98, 0xc00
	v_lshl_add_u64 v[118:119], v[118:119], 0, s[100:101]
	global_load_lds_dwordx4 v[120:121], off
	v_lshl_add_u64 v[120:121], v[120:121], 0, s[100:101]
	s_add_i32 s0, s34, 1
	s_cmp_lt_u32 s0, s35
	s_cbranch_scc0 .Lmx2_p1
	s_add_i32 m0, s98, 0x3000
	s_nop 0
	global_load_lds_dwordx4 v[106:107], off
	s_add_i32 m0, s98, 0x2000
	v_lshl_add_u64 v[106:107], v[106:107], 0, s[100:101]
	global_load_lds_dwordx4 v[108:109], off
	s_add_i32 m0, s98, 0x3400
	v_lshl_add_u64 v[108:109], v[108:109], 0, s[100:101]
	global_load_lds_dwordx4 v[110:111], off
	s_add_i32 m0, s98, 0x2400
	v_lshl_add_u64 v[110:111], v[110:111], 0, s[100:101]
	global_load_lds_dwordx4 v[112:113], off
	s_add_i32 m0, s98, 0x3800
	v_lshl_add_u64 v[112:113], v[112:113], 0, s[100:101]
	global_load_lds_dwordx4 v[114:115], off
	s_add_i32 m0, s98, 0x2800
	v_lshl_add_u64 v[114:115], v[114:115], 0, s[100:101]
	global_load_lds_dwordx4 v[116:117], off
	s_add_i32 m0, s98, 0x3c00
	v_lshl_add_u64 v[116:117], v[116:117], 0, s[100:101]
	global_load_lds_dwordx4 v[118:119], off
	s_add_i32 m0, s98, 0x2c00
	v_lshl_add_u64 v[118:119], v[118:119], 0, s[100:101]
	global_load_lds_dwordx4 v[120:121], off
	v_lshl_add_u64 v[120:121], v[120:121], 0, s[100:101]
.Lmx2_p1:
	s_branch .Lmx_pre_done

; #define LAS __attribute__((address_space(3)))
; __device__ __forceinline__ float bf_lo(unsigned w) { return __uint_as_float(w << 16); }
; __device__ __forceinline__ float bf_hi(unsigned w) { return __uint_as_float(w & 0xffff0000u); }
; #define BA_TR(off_) __builtin_bit_cast(s16x4, __builtin_amdgcn_ds_read_tr16_b64_v4i16((LAS v4i16_t*)(trb + (off_))))
; __device__ __forceinline__ void band_branch_fast(f32x16& o0, f32x16& o1, f32x4& lsum, unsigned& orw, const bf16x8 (&qf)[4], ...
;     ...
;     for (int kt = kt_lo; kt < kt_hi; ++kt) {
; #pragma unroll
;         for (int ii = 0; ii < 4; ++ii) { const int r_ = vr + 8 * ii; *(LAS v4u*)(kst + r_ * 128 + ((vc ^ (r_ & 7)) * 16)) = kn[ii]; *(LAS v4u*)(vst + r_ * 128 + vc * 16) = vn[ii]; }
;         if (kt + 1 < kt_hi) BA_LOAD(kn, vn, kt + 1);
;         bf16x8 kf[4];
; #pragma unroll
;         for (int d0 = 0; d0 < 4; ++d0) kf[d0] = *(const LAS bf16x8*)(krd + (((2 * d0 + hh) ^ (pi & 7)) * 16));
;         const LAS float* tp = tab + (kb_first + 32 * kt + tboff);
;         f32x16 s;
; #pragma unroll
;         for (int r = 0; r < 16; ++r) s[r] = tp[(r & 7) + 16 * (r >> 3)];
;         s16x4 vt[8];
; #pragma unroll
;         for (int i = 0; i < 8; ++i) vt[i] = BA_TR((i >> 2) * 2048 + ((i >> 1) & 1) * 64 + (i & 1) * 512);
;         __builtin_amdgcn_sched_barrier(0);
; #pragma unroll
;         for (int d0 = 0; d0 < 4; ++d0) s = __builtin_amdgcn_mfma_f32_32x32x16_bf16(kf[d0], qf[d0], s, 0, 0, 0);
;         __builtin_amdgcn_sched_barrier(0);
; __device__ __forceinline__ void band_state_load(f32x16& o0, f32x16& o1, float& m, float& l, const float* st, const float* ml, int lane) {
;     const int hh = lane >> 5;
;     const bf16* sb = (const bf16*)st;
; #pragma unroll
;     for (int g = 0; g < 4; ++g) { const v4u q = *(const v4u*)(sb + 32 * hh + 8 * g);
;         const auto rx = __builtin_amdgcn_permlane32_swap(q.x, q.z, false, false), ry = __builtin_amdgcn_permlane32_swap(q.y, q.w, false, false);
;         const v2u a = {rx[0], ry[0]}, b = {rx[1], ry[1]};
;         o0[4 * g] = bf_lo(a.x); o0[4 * g + 1] = bf_hi(a.x); o0[4 * g + 2] = bf_lo(a.y); o0[4 * g + 3] = bf_hi(a.y); o1[4 * g] = bf_lo(b.x); o1[4 * g + 1] = bf_hi(b.x); o1[4 * g + 2] = bf_lo(b.y); o1[4 * g + 3] = bf_hi(b.y); }
;     const f32x2 v = *(const f32x2*)ml; m = v.x; l = (hh == 0) ? v.y : 0.f;
; }
.Lmx3_p1a:
.Lmx_pre_done:
	v_lshlrev_b64 v[4:5], 3, v[182:183]
	v_or_b32_e32 v4, s44, v4
	v_lshlrev_b64 v[6:7], 8, v[4:5]
	v_lshl_add_u64 v[128:129], v[146:147], 0, v[6:7]
	v_lshl_add_u64 v[126:127], v[4:5], 3, s[12:13]
	global_load_dwordx4 v[18:21], v[128:129], off offset:48
	global_load_dwordx4 v[14:17], v[128:129], off offset:32
	global_load_dwordx4 v[10:13], v[128:129], off offset:16
	global_load_dwordx4 v[4:7], v[128:129], off
	global_load_dwordx2 v[184:185], v[126:127], off
	s_mov_b32 s0, 0x42fe0000
	s_waitcnt vmcnt(1)
	v_mov_b32_e32 v2, v6
	s_nop 1
	v_permlane32_swap_b32_e32 v4, v2
	v_mov_b32_e32 v9, v7
	v_lshlrev_b32_e32 v22, 16, v4
	v_and_b32_e32 v23, 0xffff0000, v4
	v_lshlrev_b32_e32 v6, 16, v2
	v_and_b32_e32 v7, 0xffff0000, v2
	v_mov_b32_e32 v2, v12
	v_mov_b32_e32 v4, v13
	s_nop 0
	v_permlane32_swap_b32_e32 v10, v2
	v_permlane32_swap_b32_e32 v11, v4
	v_lshlrev_b32_e32 v26, 16, v10
	v_and_b32_e32 v27, 0xffff0000, v10
	v_lshlrev_b32_e32 v28, 16, v11
	v_and_b32_e32 v29, 0xffff0000, v11
	v_lshlrev_b32_e32 v10, 16, v2
	v_and_b32_e32 v11, 0xffff0000, v2
	v_lshlrev_b32_e32 v12, 16, v4
	v_and_b32_e32 v13, 0xffff0000, v4
	v_mov_b32_e32 v2, v16
	v_mov_b32_e32 v4, v17
	s_nop 0
	v_permlane32_swap_b32_e32 v14, v2
	v_permlane32_swap_b32_e32 v15, v4
	v_lshlrev_b32_e32 v30, 16, v14
	v_and_b32_e32 v31, 0xffff0000, v14
	v_lshlrev_b32_e32 v32, 16, v15
	v_and_b32_e32 v33, 0xffff0000, v15
	v_lshlrev_b32_e32 v14, 16, v2
	v_and_b32_e32 v15, 0xffff0000, v2
	v_lshlrev_b32_e32 v16, 16, v4
	v_and_b32_e32 v17, 0xffff0000, v4
	v_mov_b32_e32 v2, v20
	v_mov_b32_e32 v4, v21
	s_nop 0
	v_permlane32_swap_b32_e32 v18, v2
	v_permlane32_swap_b32_e32 v19, v4
	v_permlane32_swap_b32_e32 v5, v9
	v_lshlrev_b32_e32 v34, 16, v18
	v_and_b32_e32 v35, 0xffff0000, v18
	v_lshlrev_b32_e32 v36, 16, v19
	v_and_b32_e32 v37, 0xffff0000, v19
	v_lshlrev_b32_e32 v18, 16, v2
	v_and_b32_e32 v19, 0xffff0000, v2
	v_cndmask_b32_e64 v2, 0, 1, s[26:27]
	v_lshlrev_b32_e32 v24, 16, v5
	v_and_b32_e32 v25, 0xffff0000, v5
	v_lshlrev_b32_e32 v8, 16, v9
	v_and_b32_e32 v9, 0xffff0000, v9
	v_lshlrev_b32_e32 v20, 16, v4
	v_and_b32_e32 v21, 0xffff0000, v4
	s_waitcnt vmcnt(0)
	v_cndmask_b32_e64 v151, 0, v185, s[6:7]
	v_cmp_neq_f32_e32 vcc, s0, v184
	v_cmp_ne_u32_e64 s[8:9], 1, v2
	s_cbranch_vccnz .LBB0_405
	s_and_b64 vcc, exec, s[8:9]
	s_mov_b64 s[10:11], -1
	s_cbranch_vccnz .LBB0_390
	s_mov_b64 s[10:11], 0
.LBB0_390:
	s_andn2_b64 vcc, exec, s[10:11]
	s_cbranch_vccnz .LBB0_395
	v_mov_b32_e32 v54, 0
	v_mov_b32_e32 v136, 0
	v_mov_b32_e32 v4, v224
	v_mov_b32_e32 v2, v223
	s_mov_b32 s0, s34
	v_mov_b32_e32 v55, v54
	v_mov_b32_e32 v56, v54
	v_mov_b32_e32 v57, v54
	s_branch .LBB0_393
.LBB0_392:
	v_add3_u32 v5, v195, v200, s99
	v_add3_u32 v38, v195, v201, s99
	ds_read_b128 v[130:133], v5 offset:20480
	ds_read_b128 v[186:189], v38 offset:20480
	v_add3_u32 v5, v195, v202, s99
	v_add3_u32 v38, v195, v203, s99
	ds_read_b128 v[226:229], v5 offset:20480
	ds_read_b128 v[230:233], v38 offset:20480
	ds_read2_b32 v[38:39], v2 offset1:1
	ds_read2_b32 v[40:41], v2 offset0:2 offset1:3
	ds_read2_b32 v[42:43], v2 offset0:4 offset1:5
	ds_read2_b32 v[44:45], v2 offset0:6 offset1:7
	ds_read2_b32 v[46:47], v2 offset0:16 offset1:17
	ds_read2_b32 v[48:49], v2 offset0:18 offset1:19
	ds_read2_b32 v[50:51], v2 offset0:20 offset1:21
	ds_read2_b32 v[52:53], v2 offset0:22 offset1:23
	v_add3_u32 v5, v194, v193, s99
	ds_read_b64_tr_b16 v[234:235], v5 offset:16384
	ds_read_b64_tr_b16 v[236:237], v5 offset:16896
	ds_read_b64_tr_b16 v[240:241], v5 offset:16960
	ds_read_b64_tr_b16 v[238:239], v5 offset:16448
	ds_read_b64_tr_b16 v[242:243], v5 offset:18432
	ds_read_b64_tr_b16 v[244:245], v5 offset:18944
	ds_read_b64_tr_b16 v[248:249], v5 offset:19008
	ds_read_b64_tr_b16 v[246:247], v5 offset:18496
	s_waitcnt lgkmcnt(8)
	v_mfma_f32_32x32x16_bf16 v[38:53], v[130:133], v[74:77], v[38:53]
	v_mfma_f32_32x32x16_bf16 v[38:53], v[186:189], v[78:81], v[38:53]
	v_mfma_f32_32x32x16_bf16 v[38:53], v[226:229], v[82:85], v[38:53]
	v_mfma_f32_32x32x16_bf16 v[38:53], v[230:233], v[86:89], v[38:53]
	s_waitcnt lgkmcnt(0)
	s_cmp_ge_u32 s0, s35
	s_cbranch_scc1 .Lmx2_last
	s_add_i32 s0, s0, 1
	s_cmp_lt_u32 s0, s35
	s_cbranch_scc0 .Lmx2_skip
	s_add_i32 m0, s98, 0x1000
	s_nop 0
	global_load_lds_dwordx4 v[106:107], off
	s_add_i32 m0, s98, 0x0
	v_lshl_add_u64 v[106:107], v[106:107], 0, s[100:101]
	global_load_lds_dwordx4 v[108:109], off
	s_add_i32 m0, s98, 0x1400
	v_lshl_add_u64 v[108:109], v[108:109], 0, s[100:101]
	global_load_lds_dwordx4 v[110:111], off
	s_add_i32 m0, s98, 0x400
	v_lshl_add_u64 v[110:111], v[110:111], 0, s[100:101]
	global_load_lds_dwordx4 v[112:113], off
	s_add_i32 m0, s98, 0x1800
	v_lshl_add_u64 v[112:113], v[112:113], 0, s[100:101]
	global_load_lds_dwordx4 v[114:115], off
	s_add_i32 m0, s98, 0x800
	v_lshl_add_u64 v[114:115], v[114:115], 0, s[100:101]
	global_load_lds_dwordx4 v[116:117], off
	s_add_i32 m0, s98, 0x1c00
	v_lshl_add_u64 v[116:117], v[116:117], 0, s[100:101]
	global_load_lds_dwordx4 v[118:119], off
	s_add_i32 m0, s98, 0xc00
	v_lshl_add_u64 v[118:119], v[118:119], 0, s[100:101]
	global_load_lds_dwordx4 v[120:121], off
	v_lshl_add_u64 v[120:121], v[120:121], 0, s[100:101]
.Lmx2_skip:
	s_add_i32 s0, s0, -1
	s_xor_b32 s98, s98, 0x2000
	s_xor_b32 s99, s99, 0x2000
	s_branch .Lmx2_join

; #define BA_PKN(a_, b_) __builtin_bit_cast(unsigned, __builtin_amdgcn_cvt_pknorm_u16((a_), (b_)))
; #define BA_PKN(a_, b_) __builtin_bit_cast(unsigned, __builtin_amdgcn_cvt_pknorm_u16((a_), (b_)))
; __device__ __forceinline__ void band_branch_fast(f32x16& o0, f32x16& o1, f32x4& lsum, unsigned& orw, const bf16x8 (&qf)[4], ...
;     ...
;         v4u p0, p1;
;     ...
;         p0.x = BA_PKN(s[0], s[1]); p0.y = BA_PKN(s[2], s[3]); p0.z = BA_PKN(s[4], s[5]); p0.w = BA_PKN(s[6], s[7]);
;         p1.x = BA_PKN(s[8], s[9]); p1.y = BA_PKN(s[10], s[11]); p1.z = BA_PKN(s[12], s[13]); p1.w = BA_PKN(s[14], s[15]);
;     ...
;         orw |= (p0.x | p0.y | p0.z) | (p0.w | p1.x | p1.y) | (p1.z | p1.w);
;         const bf16x8 pk0 = __builtin_bit_cast(bf16x8, p0), pk1 = __builtin_bit_cast(bf16x8, p1);
;         lsum = __builtin_amdgcn_mfma_f32_16x16x32_bf16(onesA, pk0, lsum, 0, 0, 0); lsum = __builtin_amdgcn_mfma_f32_16x16x32_bf16(onesA, pk1, lsum, 0, 0, 0);
;         o0 = __builtin_amdgcn_mfma_f32_32x32x16_bf16(BA_VF(0), pk0, o0, 0, 0, 0); o1 = __builtin_amdgcn_mfma_f32_32x32x16_bf16(BA_VF(2), pk0, o1, 0, 0, 0);
;         o0 = __builtin_amdgcn_mfma_f32_32x32x16_bf16(BA_VF(4), pk1, o0, 0, 0, 0); o1 = __builtin_amdgcn_mfma_f32_32x32x16_bf16(BA_VF(6), pk1, o1, 0, 0, 0);
.Lmx3_p1b:
.Lmx2_join:
	s_nop 11
	v_cvt_pknorm_u16_f32 v38, v38, v39
	v_cvt_pknorm_u16_f32 v39, v40, v41
	v_cvt_pknorm_u16_f32 v40, v42, v43
	v_cvt_pknorm_u16_f32 v41, v44, v45
	v_cvt_pknorm_u16_f32 v42, v46, v47
	v_cvt_pknorm_u16_f32 v43, v48, v49
	v_mfma_f32_32x32x16_bf16 v[22:37], v[234:237], v[38:41], v[22:37]
	v_cvt_pknorm_u16_f32 v44, v50, v51
	v_cvt_pknorm_u16_f32 v45, v52, v53
	v_or3_b32 v5, v136, v45, v44
	v_or3_b32 v5, v5, v42, v41
	v_or3_b32 v5, v5, v43, v39
	v_or3_b32 v136, v5, v38, v40
	v_add_u32_e32 v2, 0x80, v2
	v_mfma_f32_32x32x16_bf16 v[6:21], v[238:241], v[38:41], v[6:21]
	s_andn2_b64 vcc, exec, s[10:11]
	v_mfma_f32_32x32x16_bf16 v[22:37], v[242:245], v[42:45], v[22:37]
	v_mfma_f32_16x16x32_bf16 v[46:49], v[70:73], v[38:41], v[54:57]
	v_mfma_f32_32x32x16_bf16 v[6:21], v[246:249], v[42:45], v[6:21]
	v_mfma_f32_16x16x32_bf16 v[54:57], v[70:73], v[42:45], v[46:49]
	s_cbranch_vccz .LBB0_396

; __device__ __forceinline__ void mixer_a_phase(const bf16* AQ, const bf16* AK, const bf16* AV  , bf16* O, float* ST, float* ML, const float* rel_bias, LAS unsigned char* lds, int G, int blk, int tid, int lane, int wave) {
;     ...
;                 f32x4 lsum = {0.f, 0.f, 0.f, 0.f}; unsigned orw = 0u;
;                 band_branch_fast(o0, o1, lsum, orw, qf, Kb, 512, Vb, 512, 16, r, 512, 32 * (a - 2), 5, tab + 2 * TA_LEN, -(32 * a + i5) + 64 + TA_OFF + 8 * hh, vst, lane);
;                 band_branch_fast(o0, o1, lsum, orw, qf, Kb, 512, Vb, 512, 4, r & 3, 2048, 128 * a - 64, 8, tab + TA_LEN, -(128 * a + 4 * i5 + (r >> 2)) + 64 + TA_OFF + 8 * hh, vst, lane);
.LBB0_395:
	v_mov_b32_e32 v4, v3
	v_mov_b32_e32 v5, v3
	v_mov_b32_e32 v2, v3
	v_mov_b64_e32 v[56:57], v[4:5]
	v_mov_b32_e32 v136, 0
	v_mov_b64_e32 v[54:55], v[2:3]
.LBB0_396:
	v_mov_b32_e32 v2, v225
	s_mov_b32 s0, s36
	s_branch .LBB0_398
